# attention: issue 8 of the 12 K-fragment LDS reads at the very top of each trip, ahead of the next-tile global-load address setup
# speedup vs baseline: 1.0122x; 1.0051x over previous
; #define DSR(dst, addr, off) asm volatile("ds_read_b128 %0, %1 offset:%2" : "=v"(dst) : "v"(addr), "i"(off))
; __device__ __forceinline__ void attn_unit(LAS unsigned char* lds, const unsigned char* Q, const unsigned char* KV, const bf16_t* KPE, const float* CST, bf16_t* O, int b, int h, int qb, CvtState& cs) {
;     ...
;             { v4i k0, k1, k2, k3, k4, k5, k6, k7, k8, k9, k10, k11;
;               DSR(k0, ka, 0); DSR(k1, ka, 16); DSR(k2, ka, 32 * KROW); DSR(k3, ka, 32 * KROW + 16);
;               DSR(k4, ka, 64); DSR(k5, ka, 80); DSR(k6, ka, 32 * KROW + 64); DSR(k7, ka, 32 * KROW + 80);
;               DSR(k8, ka, 128); DSR(k9, ka, 144); DSR(k10, ka, 32 * KROW + 128); DSR(k11, ka, 32 * KROW + 144);
.LBB0_1028:
	s_bitcmp1_b32 s89, 0
	s_cselect_b32 s18, 0x3400, 0
	v_add_u32_e32 v82, s18, v213
	ds_read_b128 v[218:221], v82 offset:64
	ds_read_b128 v[222:225], v82 offset:0x50
	ds_read_b128 v[226:229], v82 offset:0x1a40
	ds_read_b128 v[230:233], v82 offset:0x1a50
	ds_read_b128 v[234:237], v82 offset:0x80
	ds_read_b128 v[238:241], v82 offset:0x90
	ds_read_b128 v[242:245], v82 offset:0x1a80
	ds_read_b128 v[246:249], v82 offset:0x1a90
	s_add_i32 s88, s89, 1
	s_cmp_lt_u32 s88, s33
	s_cselect_b64 s[44:45], -1, 0
	s_cmp_ge_u32 s88, s33
	s_cbranch_scc1 .LBB0_1043
	v_lshl_add_u64 v[74:75], s[12:13], 0, v[190:191]
	v_add_co_u32_e32 v74, vcc, 0x20000, v74
	s_waitcnt vmcnt(8)
	v_mov_b32_e32 v207, v191
	v_addc_co_u32_e32 v75, vcc, 0, v75, vcc
	global_load_dwordx2 v[196:197], v190, s[12:13]
	global_load_dwordx2 v[198:199], v[74:75], off
	global_load_dwordx4 v[154:157], v216, s[4:5]
	v_lshl_add_u64 v[74:75], s[12:13], 0, v[206:207]
	v_add_co_u32_e32 v76, vcc, 0x1000, v74
	global_load_dword v193, v206, s[12:13]
	s_nop 0
	v_addc_co_u32_e32 v77, vcc, 0, v75, vcc
	global_load_dword v195, v[76:77], off
	v_add_co_u32_e32 v76, vcc, 0x2000, v74
	s_nop 1
	v_addc_co_u32_e32 v77, vcc, 0, v75, vcc
	v_add_co_u32_e32 v74, vcc, 0x3000, v74
	global_load_dword v207, v[76:77], off
	s_nop 0
	v_addc_co_u32_e32 v75, vcc, 0, v75, vcc
	global_load_dword v211, v[74:75], off
	s_andn2_b64 vcc, exec, s[46:47]
	s_cbranch_vccz .LBB0_1044

;     __device__ __forceinline__ bool next(int i, Unit& u) const { if (!T.tile(i, u.pm, u.pn)) return false; u.aoff = (size_t)u.pm * atile; u.boff = (size_t)u.pn * btile; return true; }
;     __device__ __forceinline__ bool next(int i, Unit& u) const { if (!T.tile(i, u.pm, u.pn)) return false; u.aoff = (size_t)u.pm * 256 * D * 2 + (size_t)(u.pn >> 1) * 512; u.boff = (size_t)u.pn * 256 * 256 * 2; return true; }
;     __device__ __forceinline__ bool next(int i, Unit& u) const { if (!T.tile(i, u.pm, u.pn)) return false; const int e = tile_e[u.pm] & 7; u.aoff = (size_t)u.pm * atile; u.boff = ((size_t)e * nN + u.pn) * btile; return true; }
; __device__ __forceinline__ void cvt_load(const CvtState& cs, int lane, f32x4 (&v)[8]) {
;     const int kb = cs.next % CV_KB, tmp = cs.next / CV_KB, nb = tmp % CV_NB, e = tmp / CV_NB;
;     const float* src = cs.W + ((size_t)e * FF + (size_t)(128 * kb + 8 * (lane >> 2))) * D + 16 * nb + 4 * (lane & 3);
; #pragma unroll
;     for (int i = 0; i < 8; ++i) v[i] = *(const f32x4*)(src + (size_t)i * D);
; }
; __device__ __forceinline__ void attn_unit(LAS unsigned char* lds, const unsigned char* Q, const unsigned char* KV, const bf16_t* KPE, const float* CST, bf16_t* O, int b, int h, int qb, CvtState& cs) {
;     ...
;         if (kb0 <= qlo + 31) {
;             const unsigned ka = (unsigned)(uintptr_t)lds + (unsigned)((t & 1) * KBUF + r32 * KROW + hi * 32);
;             f32x16 p0, p1;
; #pragma unroll
;             for (int r = 0; r < 16; ++r) { p0[r] = 0.f; p1[r] = 0.f; }
;             { v4i k0, k1, k2, k3, k4, k5, k6, k7, k8, k9, k10, k11;
;               DSR(k0, ka, 0); DSR(k1, ka, 16); DSR(k2, ka, 32 * KROW); DSR(k3, ka, 32 * KROW + 16);
;               DSR(k4, ka, 64); DSR(k5, ka, 80); DSR(k6, ka, 32 * KROW + 64); DSR(k7, ka, 32 * KROW + 80);
;               DSR(k8, ka, 128); DSR(k9, ka, 144); DSR(k10, ka, 32 * KROW + 128); DSR(k11, ka, 32 * KROW + 144);
;               DSW4(8, k0, k1, k2, k3);
;               p0 = MMA8(CAT8(k0, k1), qf[0], p0); p1 = MMA8(CAT8(k2, k3), qf[0], p1);
;               PV_READ(vs);
;               DSW4(12, k4, k5, k6, k7);
;               p0 = MMA8(CAT8(k4, k5), qf[1], p0); p1 = MMA8(CAT8(k6, k7), qf[1], p1);
;               DSW4(8, k8, k9, k10, k11);
;               p0 = MMA8(CAT8(k8, k9), qf[2], p0); p1 = MMA8(CAT8(k10, k11), qf[2], p1); }
;             if (cvt_now) cvt_load(cs, lane, cv);
.LBB0_1034:
	s_andn2_b64 vcc, exec, s[48:49]
	s_cbranch_vccnz .LBB0_1047
	s_bitcmp1_b32 s89, 0
	s_cselect_b32 s18, 0x3400, 0
	v_add_u32_e32 v82, s18, v213
	ds_read_b128 v[66:69], v82 offset:0
	ds_read_b128 v[70:73], v82 offset:16
	ds_read_b128 v[74:77], v82 offset:0x1a00
	ds_read_b128 v[78:81], v82 offset:0x1a10
	s_nop 0
	s_waitcnt lgkmcnt(0)
	s_mul_i32 s18, s79, 0x2800
	v_mfma_f32_32x32x64_f8f6f4 v[82:97], v[66:73], v[98:105], 0
	v_add_u32_e32 v126, s18, v214
	ds_read_b128 v[146:149], v126 offset:0
	ds_read_b128 v[150:153], v126 offset:16
	ds_read_b128 v[138:141], v126 offset:0xa00
	ds_read_b128 v[142:145], v126 offset:0xa10
	ds_read_b128 v[130:133], v126 offset:0x1400
	ds_read_b128 v[134:137], v126 offset:0x1410
	ds_read_b128 v[122:125], v126 offset:0x1e00
	ds_read_b128 v[126:129], v126 offset:0x1e10
	s_waitcnt lgkmcnt(12)
	s_waitcnt lgkmcnt(8)
	s_andn2_b64 vcc, exec, s[46:47]
	v_mfma_f32_32x32x64_f8f6f4 v[66:81], v[74:81], v[98:105], 0
	v_mfma_f32_32x32x64_f8f6f4 v[82:97], v[218:225], v[106:113], v[82:97]
	v_mfma_f32_32x32x64_f8f6f4 v[66:81], v[226:233], v[106:113], v[66:81]
	v_mfma_f32_32x32x64_f8f6f4 v[82:97], v[234:241], v[114:121], v[82:97]
	v_mfma_f32_32x32x64_f8f6f4 v[66:81], v[242:249], v[114:121], v[66:81]
	s_cbranch_vccnz .LBB0_1037
	s_mul_hi_i32 s18, s35, 0x92492493
	s_add_i32 s18, s18, s35
	s_ashr_i32 s19, s18, 5
	s_lshr_b32 s20, s18, 31
	s_add_i32 s19, s19, s20
	s_mul_i32 s21, s19, 56
	s_ashr_i32 s48, s19, 31
	s_sub_i32 s21, s35, s21
	s_lshr_b32 s48, s48, 25
	s_add_i32 s48, s19, s48
	s_ashr_i32 s18, s18, 12
	s_waitcnt vmcnt(7)
	v_lshl_or_b32 v158, s21, 7, v204
	s_and_b32 s48, s48, 0xfffff80
	s_add_i32 s18, s18, s20
	v_ashrrev_i32_e32 v159, 31, v158
	s_sub_i32 s48, s19, s48
	v_mad_i64_i32 v[158:159], s[18:19], s18, v208, v[158:159]
	v_lshlrev_b64 v[158:159], 13, v[158:159]
	s_lshl_b32 s18, s48, 4
	v_lshl_add_u64 v[158:159], s[26:27], 0, v[158:159]
	s_ashr_i32 s19, s18, 31
	v_lshl_add_u64 v[158:159], s[18:19], 2, v[158:159]
	v_lshlrev_b32_e32 v160, 2, v202
	v_mov_b32_e32 v161, v191
	s_waitcnt vmcnt(7)
	v_lshl_add_u64 v[182:183], v[158:159], 0, v[160:161]
	v_add_co_u32_e32 v162, vcc, s52, v182
	s_nop 1
	v_addc_co_u32_e32 v163, vcc, 0, v183, vcc
	v_add_co_u32_e32 v166, vcc, s62, v182
	global_load_dwordx4 v[158:161], v[182:183], off
	s_nop 0
	global_load_dwordx4 v[162:165], v[162:163], off
	v_addc_co_u32_e32 v167, vcc, 0, v183, vcc
	v_add_co_u32_e32 v170, vcc, s63, v182
	s_nop 1
	v_addc_co_u32_e32 v171, vcc, 0, v183, vcc
	v_add_co_u32_e32 v174, vcc, s64, v182
	global_load_dwordx4 v[166:169], v[166:167], off
	s_nop 0
	global_load_dwordx4 v[170:173], v[170:171], off
	v_addc_co_u32_e32 v175, vcc, 0, v183, vcc
	v_add_co_u32_e32 v178, vcc, s65, v182
	s_nop 1
	v_addc_co_u32_e32 v179, vcc, 0, v183, vcc
	v_add_co_u32_e32 v184, vcc, s66, v182
	global_load_dwordx4 v[174:177], v[174:175], off
	s_nop 0
	global_load_dwordx4 v[178:181], v[178:179], off
	v_addc_co_u32_e32 v185, vcc, 0, v183, vcc
	s_waitcnt vmcnt(13)
	v_add_co_u32_e32 v186, vcc, s67, v182
	s_nop 1
	v_addc_co_u32_e32 v187, vcc, 0, v183, vcc
	global_load_dwordx4 v[182:185], v[184:185], off
	s_nop 0
	global_load_dwordx4 v[186:189], v[186:187], off
